# GDN section c: the twenty non-zero LM / qk tiles dealt over all eight waves (max three per wave), zero qk tiles stored by wave 7
# baseline (speedup 1.0000x reference)
.Lgpf_done_next:
	v_and_b32_e32 v0, 15, v215
	v_lshrrev_b32_e32 v1, 4, v215
	v_mul_u32_u24_e32 v4, 0x110, v0
	v_lshl_add_u32 v4, v1, 4, v4
	v_lshlrev_b32_e32 v6, 2, v0
	v_add_u32_e32 v6, 0x1c400, v6
	v_lshlrev_b32_e32 v7, 4, v0
	v_and_b32_e32 v2, 1, v1
	v_lshl_add_u32 v7, v2, 9, v7
	v_lshrrev_b32_e32 v2, 1, v1
	v_lshl_add_u32 v7, v2, 3, v7
	s_add_u32 s2, s78, 0xc000
	s_addc_u32 s3, s79, 0
	s_cmp_eq_u32 s10, 16
	s_cbranch_scc1 .Lgc_w1
	s_cmp_eq_u32 s10, 32
	s_cbranch_scc1 .Lgc_w2
	s_cmp_eq_u32 s10, 48
	s_cbranch_scc1 .Lgc_w3
	s_cmp_eq_u32 s10, 64
	s_cbranch_scc1 .Lgc_w4
	s_cmp_eq_u32 s10, 80
	s_cbranch_scc1 .Lgc_w5
	s_cmp_eq_u32 s10, 96
	s_cbranch_scc1 .Lgc_w6
	s_cmp_eq_u32 s10, 112
	s_cbranch_scc1 .Lgc_w7
	s_mov_b32 s34, 0x3fb8aa3b
	v_add_u32_e32 v3, 0x4400, v4
	v_lshlrev_b32_e32 v5, 4, v1
	v_add_u32_e32 v5, 0x1c400, v5
	ds_read_b128 v[40:43], v3
	ds_read_b128 v[44:47], v3 offset:64
	ds_read_b128 v[48:51], v3 offset:128
	ds_read_b128 v[52:55], v3 offset:192
	ds_read_b128 v[56:59], v4
	ds_read_b128 v[60:63], v4 offset:64
	ds_read_b128 v[64:67], v4 offset:128
	ds_read_b128 v[68:71], v4 offset:192
	ds_read_b128 v[144:147], v5
	ds_read_b32 v136, v6
	v_lshl_add_u32 v12, v1, 2, 0
	v_add_u32_e32 v13, 1, v12
	v_add_u32_e32 v14, 2, v12
	v_add_u32_e32 v15, 3, v12
	s_waitcnt lgkmcnt(0)
	v_mfma_f32_16x16x32_bf16 v[120:123], v[40:43], v[56:59], 0
	v_mfma_f32_16x16x32_bf16 v[120:123], v[44:47], v[60:63], v[120:123]
	v_mfma_f32_16x16x32_bf16 v[120:123], v[48:51], v[64:67], v[120:123]
	v_mfma_f32_16x16x32_bf16 v[120:123], v[52:55], v[68:71], v[120:123]
	v_sub_f32_e32 v148, v144, v136
	v_sub_f32_e32 v149, v145, v136
	v_sub_f32_e32 v150, v146, v136
	v_sub_f32_e32 v151, v147, v136
	v_mul_f32_e32 v148, s34, v148
	v_mul_f32_e32 v149, s34, v149
	v_mul_f32_e32 v150, s34, v150
	v_mul_f32_e32 v151, s34, v151
	v_exp_f32_e32 v148, v148
	v_exp_f32_e32 v149, v149
	v_exp_f32_e32 v150, v150
	v_exp_f32_e32 v151, v151
	v_mul_f32_e32 v148, v120, v148
	v_mul_f32_e32 v149, v121, v149
	v_mul_f32_e32 v150, v122, v150
	v_mul_f32_e32 v151, v123, v151
	v_cmp_lt_i32_e32 vcc, v0, v12
	v_cmp_lt_i32_e64 s[0:1], v0, v13
	v_cmp_lt_i32_e64 s[20:21], v0, v14
	v_cndmask_b32_e32 v148, 0, v148, vcc
	v_cmp_lt_i32_e32 vcc, v0, v15
	v_cndmask_b32_e64 v149, 0, v149, s[0:1]
	v_cndmask_b32_e64 v150, 0, v150, s[20:21]
	s_nop 0
	v_cndmask_b32_e32 v151, 0, v151, vcc
	v_add_u32_e32 v16, 0x15c00, v4
	ds_write_b128 v16, v[148:151]
	s_branch .Lgc_join
.Lgc_w1:
	s_mov_b32 s34, 0x3fb8aa3b
	v_add_u32_e32 v3, 0x5500, v4
	v_lshlrev_b32_e32 v5, 4, v1
	v_add_u32_e32 v5, 0x1c440, v5
	ds_read_b128 v[40:43], v3
	ds_read_b128 v[44:47], v3 offset:64
	ds_read_b128 v[48:51], v3 offset:128
	ds_read_b128 v[52:55], v3 offset:192
	ds_read_b128 v[56:59], v4
	ds_read_b128 v[60:63], v4 offset:64
	ds_read_b128 v[64:67], v4 offset:128
	ds_read_b128 v[68:71], v4 offset:192
	ds_read_b128 v[144:147], v5
	ds_read_b32 v136, v6
	ds_read_b32 v137, v6 offset:64
	ds_read_b128 v[72:75], v4 offset:4352
	ds_read_b128 v[76:79], v4 offset:4416
	ds_read_b128 v[80:83], v4 offset:4480
	ds_read_b128 v[84:87], v4 offset:4544
	v_add_u32_e32 v9, 16, v0
	v_lshl_add_u32 v12, v1, 2, 16
	v_add_u32_e32 v13, 1, v12
	v_add_u32_e32 v14, 2, v12
	v_add_u32_e32 v15, 3, v12
	s_waitcnt lgkmcnt(5)
	v_mfma_f32_16x16x32_bf16 v[120:123], v[40:43], v[56:59], 0
	v_mfma_f32_16x16x32_bf16 v[120:123], v[44:47], v[60:63], v[120:123]
	v_mfma_f32_16x16x32_bf16 v[120:123], v[48:51], v[64:67], v[120:123]
	v_mfma_f32_16x16x32_bf16 v[120:123], v[52:55], v[68:71], v[120:123]
	v_sub_f32_e32 v148, v144, v136
	v_sub_f32_e32 v149, v145, v136
	v_sub_f32_e32 v150, v146, v136
	v_sub_f32_e32 v151, v147, v136
	v_mul_f32_e32 v148, s34, v148
	v_mul_f32_e32 v149, s34, v149
	v_mul_f32_e32 v150, s34, v150
	v_mul_f32_e32 v151, s34, v151
	v_exp_f32_e32 v148, v148
	v_exp_f32_e32 v149, v149
	v_exp_f32_e32 v150, v150
	v_exp_f32_e32 v151, v151
	s_waitcnt lgkmcnt(0)
	v_mfma_f32_16x16x32_bf16 v[124:127], v[40:43], v[72:75], 0
	v_mfma_f32_16x16x32_bf16 v[124:127], v[44:47], v[76:79], v[124:127]
	v_mfma_f32_16x16x32_bf16 v[124:127], v[48:51], v[80:83], v[124:127]
	v_mfma_f32_16x16x32_bf16 v[124:127], v[52:55], v[84:87], v[124:127]
	v_mul_f32_e32 v148, v120, v148
	v_mul_f32_e32 v149, v121, v149
	v_mul_f32_e32 v150, v122, v150
	v_mul_f32_e32 v151, v123, v151
	v_sub_f32_e32 v152, v144, v137
	v_sub_f32_e32 v153, v145, v137
	v_sub_f32_e32 v154, v146, v137
	v_sub_f32_e32 v155, v147, v137
	v_mul_f32_e32 v152, s34, v152
	v_mul_f32_e32 v153, s34, v153
	v_mul_f32_e32 v154, s34, v154
	v_mul_f32_e32 v155, s34, v155
	v_exp_f32_e32 v152, v152
	v_exp_f32_e32 v153, v153
	v_exp_f32_e32 v154, v154
	v_exp_f32_e32 v155, v155
	v_mul_f32_e32 v152, v124, v152
	v_mul_f32_e32 v153, v125, v153
	v_mul_f32_e32 v154, v126, v154
	v_mul_f32_e32 v155, v127, v155
	v_cmp_lt_i32_e32 vcc, v9, v12
	v_cmp_lt_i32_e64 s[0:1], v9, v13
	v_cmp_lt_i32_e64 s[20:21], v9, v14
	v_cndmask_b32_e32 v152, 0, v152, vcc
	v_cmp_lt_i32_e32 vcc, v9, v15
	v_cndmask_b32_e64 v153, 0, v153, s[0:1]
	v_cndmask_b32_e64 v154, 0, v154, s[20:21]
	s_nop 0
	v_cndmask_b32_e32 v155, 0, v155, vcc
	v_add_u32_e32 v16, 0x15c40, v4
	ds_write_b128 v16, v[148:151]
	ds_write_b128 v16, v[152:155] offset:4352
	s_mov_b32 s34, 0xbfb8aa3b
	v_add_u32_e32 v3, 0x3300, v4
	v_add_u32_e32 v2, 0x8800, v4
	v_lshlrev_b32_e32 v5, 4, v1
	v_add_u32_e32 v5, 0x1c4c0, v5
	ds_read_b128 v[40:43], v3
	ds_read_b128 v[44:47], v3 offset:64
	ds_read_b128 v[48:51], v3 offset:128
	ds_read_b128 v[52:55], v3 offset:192
	ds_read_b128 v[104:107], v2 offset:13056
	ds_read_b128 v[108:111], v2 offset:13120
	ds_read_b128 v[112:115], v2 offset:13184
	ds_read_b128 v[116:119], v2 offset:13248
	ds_read_b128 v[144:147], v5
	ds_read_b32 v139, v6 offset:192
	v_add_u32_e32 v11, 48, v0
	v_lshl_add_u32 v12, v1, 2, 48
	v_add_u32_e32 v13, 1, v12
	v_add_u32_e32 v14, 2, v12
	v_add_u32_e32 v15, 3, v12
	s_waitcnt lgkmcnt(0)
	v_mfma_f32_16x16x32_bf16 v[132:135], v[40:43], v[104:107], 0
	v_mfma_f32_16x16x32_bf16 v[132:135], v[44:47], v[108:111], v[132:135]
	v_mfma_f32_16x16x32_bf16 v[132:135], v[48:51], v[112:115], v[132:135]
	v_mfma_f32_16x16x32_bf16 v[132:135], v[52:55], v[116:119], v[132:135]
	v_sub_f32_e32 v160, v144, v139
	v_sub_f32_e32 v161, v145, v139
	v_sub_f32_e32 v162, v146, v139
	v_sub_f32_e32 v163, v147, v139
	v_mul_f32_e32 v160, s34, v160
	v_mul_f32_e32 v161, s34, v161
	v_mul_f32_e32 v162, s34, v162
	v_mul_f32_e32 v163, s34, v163
	v_exp_f32_e32 v160, v160
	v_exp_f32_e32 v161, v161
	v_exp_f32_e32 v162, v162
	v_exp_f32_e32 v163, v163
	v_mul_f32_e32 v160, v132, v160
	v_mul_f32_e32 v161, v133, v161
	v_mul_f32_e32 v162, v134, v162
	v_mul_f32_e32 v163, v135, v163
	v_cmp_le_i32_e32 vcc, v12, v11
	v_cmp_le_i32_e64 s[0:1], v13, v11
	v_cmp_le_i32_e64 s[20:21], v14, v11
	v_cndmask_b32_e32 v160, 0, v160, vcc
	v_cmp_le_i32_e32 vcc, v15, v11
	v_cndmask_b32_e64 v161, 0, v161, s[0:1]
	v_cndmask_b32_e64 v162, 0, v162, s[20:21]
	s_nop 0
	v_cndmask_b32_e32 v163, 0, v163, vcc
	v_cvt_pk_bf16_f32 v170, v160, v161
	v_cvt_pk_bf16_f32 v171, v162, v163
	v_add_u32_e32 v16, 0xc00, v7
	v_add_u32_e32 v17, 0x1000, v16
	global_store_dwordx2 v17, v[170:171], s[2:3] offset:256
	s_branch .Lgc_join
.Lgc_w2:
	s_mov_b32 s34, 0x3fb8aa3b
	v_add_u32_e32 v3, 0x6600, v4
	v_lshlrev_b32_e32 v5, 4, v1
	v_add_u32_e32 v5, 0x1c480, v5
	ds_read_b128 v[40:43], v3
	ds_read_b128 v[44:47], v3 offset:64
	ds_read_b128 v[48:51], v3 offset:128
	ds_read_b128 v[52:55], v3 offset:192
	ds_read_b128 v[56:59], v4
	ds_read_b128 v[60:63], v4 offset:64
	ds_read_b128 v[64:67], v4 offset:128
	ds_read_b128 v[68:71], v4 offset:192
	ds_read_b128 v[144:147], v5
	ds_read_b32 v136, v6
	ds_read_b32 v137, v6 offset:64
	ds_read_b128 v[72:75], v4 offset:4352
	ds_read_b128 v[76:79], v4 offset:4416
	ds_read_b128 v[80:83], v4 offset:4480
	ds_read_b128 v[84:87], v4 offset:4544
	s_waitcnt lgkmcnt(5)
	v_mfma_f32_16x16x32_bf16 v[120:123], v[40:43], v[56:59], 0
	v_mfma_f32_16x16x32_bf16 v[120:123], v[44:47], v[60:63], v[120:123]
	v_mfma_f32_16x16x32_bf16 v[120:123], v[48:51], v[64:67], v[120:123]
	v_mfma_f32_16x16x32_bf16 v[120:123], v[52:55], v[68:71], v[120:123]
	v_sub_f32_e32 v148, v144, v136
	v_sub_f32_e32 v149, v145, v136
	v_sub_f32_e32 v150, v146, v136
	v_sub_f32_e32 v151, v147, v136
	v_mul_f32_e32 v148, s34, v148
	v_mul_f32_e32 v149, s34, v149
	v_mul_f32_e32 v150, s34, v150
	v_mul_f32_e32 v151, s34, v151
	v_exp_f32_e32 v148, v148
	v_exp_f32_e32 v149, v149
	v_exp_f32_e32 v150, v150
	v_exp_f32_e32 v151, v151
	s_waitcnt lgkmcnt(0)
	v_mfma_f32_16x16x32_bf16 v[124:127], v[40:43], v[72:75], 0
	v_mfma_f32_16x16x32_bf16 v[124:127], v[44:47], v[76:79], v[124:127]
	v_mfma_f32_16x16x32_bf16 v[124:127], v[48:51], v[80:83], v[124:127]
	v_mfma_f32_16x16x32_bf16 v[124:127], v[52:55], v[84:87], v[124:127]
	v_mul_f32_e32 v148, v120, v148
	v_mul_f32_e32 v149, v121, v149
	v_mul_f32_e32 v150, v122, v150
	v_mul_f32_e32 v151, v123, v151
	v_sub_f32_e32 v152, v144, v137
	v_sub_f32_e32 v153, v145, v137
	v_sub_f32_e32 v154, v146, v137
	v_sub_f32_e32 v155, v147, v137
	v_mul_f32_e32 v152, s34, v152
	v_mul_f32_e32 v153, s34, v153
	v_mul_f32_e32 v154, s34, v154
	v_mul_f32_e32 v155, s34, v155
	v_exp_f32_e32 v152, v152
	v_exp_f32_e32 v153, v153
	v_exp_f32_e32 v154, v154
	v_exp_f32_e32 v155, v155
	v_mul_f32_e32 v152, v124, v152
	v_mul_f32_e32 v153, v125, v153
	v_mul_f32_e32 v154, v126, v154
	v_mul_f32_e32 v155, v127, v155
	v_add_u32_e32 v16, 0x15c80, v4
	ds_write_b128 v16, v[148:151]
	ds_write_b128 v16, v[152:155] offset:4352
	v_mul_u32_u24_e32 v17, 0x140, v1
	v_lshl_add_u32 v17, v0, 1, v17
	v_add_u32_e32 v17, 0x1c800, v17
	v_cvt_pk_bf16_f32 v164, v148, v148
	v_cvt_pk_bf16_f32 v165, v149, v149
	v_cvt_pk_bf16_f32 v166, v150, v150
	v_cvt_pk_bf16_f32 v167, v151, v151
	v_cvt_pk_bf16_f32 v168, v152, v152
	v_cvt_pk_bf16_f32 v169, v153, v153
	v_cvt_pk_bf16_f32 v170, v154, v154
	v_cvt_pk_bf16_f32 v171, v155, v155
	ds_write_b16 v17, v164
	ds_write_b16 v17, v165 offset:80
	ds_write_b16 v17, v166 offset:160
	ds_write_b16 v17, v167 offset:240
	ds_write_b16 v17, v168 offset:32
	ds_write_b16 v17, v169 offset:112
	ds_write_b16 v17, v170 offset:192
	ds_write_b16 v17, v171 offset:272
	s_branch .Lgc_join
.Lgc_w3:
	s_mov_b32 s34, 0x3fb8aa3b
	v_add_u32_e32 v3, 0x7700, v4
	v_lshlrev_b32_e32 v5, 4, v1
	v_add_u32_e32 v5, 0x1c4c0, v5
	ds_read_b128 v[40:43], v3
	ds_read_b128 v[44:47], v3 offset:64
	ds_read_b128 v[48:51], v3 offset:128
	ds_read_b128 v[52:55], v3 offset:192
	ds_read_b128 v[56:59], v4
	ds_read_b128 v[60:63], v4 offset:64
	ds_read_b128 v[64:67], v4 offset:128
	ds_read_b128 v[68:71], v4 offset:192
	ds_read_b128 v[144:147], v5
	ds_read_b32 v136, v6
	ds_read_b32 v137, v6 offset:64
	ds_read_b32 v138, v6 offset:128
	ds_read_b128 v[72:75], v4 offset:4352
	ds_read_b128 v[76:79], v4 offset:4416
	ds_read_b128 v[80:83], v4 offset:4480
	ds_read_b128 v[84:87], v4 offset:4544
	ds_read_b128 v[88:91], v4 offset:8704
	ds_read_b128 v[92:95], v4 offset:8768
	ds_read_b128 v[96:99], v4 offset:8832
	ds_read_b128 v[100:103], v4 offset:8896
	s_waitcnt lgkmcnt(10)
	v_mfma_f32_16x16x32_bf16 v[120:123], v[40:43], v[56:59], 0
	v_mfma_f32_16x16x32_bf16 v[120:123], v[44:47], v[60:63], v[120:123]
	v_mfma_f32_16x16x32_bf16 v[120:123], v[48:51], v[64:67], v[120:123]
	v_mfma_f32_16x16x32_bf16 v[120:123], v[52:55], v[68:71], v[120:123]
	v_sub_f32_e32 v148, v144, v136
	v_sub_f32_e32 v149, v145, v136
	v_sub_f32_e32 v150, v146, v136
	v_sub_f32_e32 v151, v147, v136
	v_mul_f32_e32 v148, s34, v148
	v_mul_f32_e32 v149, s34, v149
	v_mul_f32_e32 v150, s34, v150
	v_mul_f32_e32 v151, s34, v151
	v_exp_f32_e32 v148, v148
	v_exp_f32_e32 v149, v149
	v_exp_f32_e32 v150, v150
	v_exp_f32_e32 v151, v151
	s_waitcnt lgkmcnt(4)
	v_mfma_f32_16x16x32_bf16 v[124:127], v[40:43], v[72:75], 0
	v_mfma_f32_16x16x32_bf16 v[124:127], v[44:47], v[76:79], v[124:127]
	v_mfma_f32_16x16x32_bf16 v[124:127], v[48:51], v[80:83], v[124:127]
	v_mfma_f32_16x16x32_bf16 v[124:127], v[52:55], v[84:87], v[124:127]
	v_mul_f32_e32 v148, v120, v148
	v_mul_f32_e32 v149, v121, v149
	v_mul_f32_e32 v150, v122, v150
	v_mul_f32_e32 v151, v123, v151
	v_sub_f32_e32 v152, v144, v137
	v_sub_f32_e32 v153, v145, v137
	v_sub_f32_e32 v154, v146, v137
	v_sub_f32_e32 v155, v147, v137
	v_mul_f32_e32 v152, s34, v152
	v_mul_f32_e32 v153, s34, v153
	v_mul_f32_e32 v154, s34, v154
	v_mul_f32_e32 v155, s34, v155
	v_exp_f32_e32 v152, v152
	v_exp_f32_e32 v153, v153
	v_exp_f32_e32 v154, v154
	v_exp_f32_e32 v155, v155
	s_waitcnt lgkmcnt(0)
	v_mfma_f32_16x16x32_bf16 v[128:131], v[40:43], v[88:91], 0
	v_mfma_f32_16x16x32_bf16 v[128:131], v[44:47], v[92:95], v[128:131]
	v_mfma_f32_16x16x32_bf16 v[128:131], v[48:51], v[96:99], v[128:131]
	v_mfma_f32_16x16x32_bf16 v[128:131], v[52:55], v[100:103], v[128:131]
	v_mul_f32_e32 v152, v124, v152
	v_mul_f32_e32 v153, v125, v153
	v_mul_f32_e32 v154, v126, v154
	v_mul_f32_e32 v155, v127, v155
	v_sub_f32_e32 v156, v144, v138
	v_sub_f32_e32 v157, v145, v138
	v_sub_f32_e32 v158, v146, v138
	v_sub_f32_e32 v159, v147, v138
	v_mul_f32_e32 v156, s34, v156
	v_mul_f32_e32 v157, s34, v157
	v_mul_f32_e32 v158, s34, v158
	v_mul_f32_e32 v159, s34, v159
	v_exp_f32_e32 v156, v156
	v_exp_f32_e32 v157, v157
	v_exp_f32_e32 v158, v158
	v_exp_f32_e32 v159, v159
	v_mul_f32_e32 v156, v128, v156
	v_mul_f32_e32 v157, v129, v157
	v_mul_f32_e32 v158, v130, v158
	v_mul_f32_e32 v159, v131, v159
	v_add_u32_e32 v16, 0x15cc0, v4
	ds_write_b128 v16, v[148:151]
	ds_write_b128 v16, v[152:155] offset:4352
	ds_write_b128 v16, v[156:159] offset:8704
	v_mul_u32_u24_e32 v17, 0x140, v1
	v_lshl_add_u32 v17, v0, 1, v17
	v_add_u32_e32 v17, 0x1cd00, v17
	v_cvt_pk_bf16_f32 v164, v148, v148
	v_cvt_pk_bf16_f32 v165, v149, v149
	v_cvt_pk_bf16_f32 v166, v150, v150
	v_cvt_pk_bf16_f32 v167, v151, v151
	v_cvt_pk_bf16_f32 v168, v152, v152
	v_cvt_pk_bf16_f32 v169, v153, v153
	v_cvt_pk_bf16_f32 v170, v154, v154
	v_cvt_pk_bf16_f32 v171, v155, v155
	ds_write_b16 v17, v164
	ds_write_b16 v17, v165 offset:80
	ds_write_b16 v17, v166 offset:160
	ds_write_b16 v17, v167 offset:240
	ds_write_b16 v17, v168 offset:32
	ds_write_b16 v17, v169 offset:112
	ds_write_b16 v17, v170 offset:192
	ds_write_b16 v17, v171 offset:272
	s_branch .Lgc_join
.Lgc_w4:
	s_mov_b32 s34, 0xbfb8aa3b
	v_add_u32_e32 v3, 0x0, v4
	v_add_u32_e32 v2, 0x8800, v4
	v_lshlrev_b32_e32 v5, 4, v1
	v_add_u32_e32 v5, 0x1c400, v5
	ds_read_b128 v[40:43], v3
	ds_read_b128 v[44:47], v3 offset:64
	ds_read_b128 v[48:51], v3 offset:128
	ds_read_b128 v[52:55], v3 offset:192
	ds_read_b128 v[56:59], v2
	ds_read_b128 v[60:63], v2 offset:64
	ds_read_b128 v[64:67], v2 offset:128
	ds_read_b128 v[68:71], v2 offset:192
	ds_read_b128 v[144:147], v5
	ds_read_b32 v136, v6
	ds_read_b32 v137, v6 offset:64
	ds_read_b32 v138, v6 offset:128
	ds_read_b128 v[72:75], v2 offset:4352
	ds_read_b128 v[76:79], v2 offset:4416
	ds_read_b128 v[80:83], v2 offset:4480
	ds_read_b128 v[84:87], v2 offset:4544
	ds_read_b128 v[88:91], v2 offset:8704
	ds_read_b128 v[92:95], v2 offset:8768
	ds_read_b128 v[96:99], v2 offset:8832
	ds_read_b128 v[100:103], v2 offset:8896
	v_lshl_add_u32 v12, v1, 2, 0
	v_add_u32_e32 v13, 1, v12
	v_add_u32_e32 v14, 2, v12
	v_add_u32_e32 v15, 3, v12
	s_waitcnt lgkmcnt(10)
	v_mfma_f32_16x16x32_bf16 v[120:123], v[40:43], v[56:59], 0
	v_mfma_f32_16x16x32_bf16 v[120:123], v[44:47], v[60:63], v[120:123]
	v_mfma_f32_16x16x32_bf16 v[120:123], v[48:51], v[64:67], v[120:123]
	v_mfma_f32_16x16x32_bf16 v[120:123], v[52:55], v[68:71], v[120:123]
	v_sub_f32_e32 v148, v144, v136
	v_sub_f32_e32 v149, v145, v136
	v_sub_f32_e32 v150, v146, v136
	v_sub_f32_e32 v151, v147, v136
	v_mul_f32_e32 v148, s34, v148
	v_mul_f32_e32 v149, s34, v149
	v_mul_f32_e32 v150, s34, v150
	v_mul_f32_e32 v151, s34, v151
	v_exp_f32_e32 v148, v148
	v_exp_f32_e32 v149, v149
	v_exp_f32_e32 v150, v150
	v_exp_f32_e32 v151, v151
	s_waitcnt lgkmcnt(4)
	v_mfma_f32_16x16x32_bf16 v[124:127], v[40:43], v[72:75], 0
	v_mfma_f32_16x16x32_bf16 v[124:127], v[44:47], v[76:79], v[124:127]
	v_mfma_f32_16x16x32_bf16 v[124:127], v[48:51], v[80:83], v[124:127]
	v_mfma_f32_16x16x32_bf16 v[124:127], v[52:55], v[84:87], v[124:127]
	v_mul_f32_e32 v148, v120, v148
	v_mul_f32_e32 v149, v121, v149
	v_mul_f32_e32 v150, v122, v150
	v_mul_f32_e32 v151, v123, v151
	v_cmp_le_i32_e32 vcc, v12, v0
	v_cmp_le_i32_e64 s[0:1], v13, v0
	v_cmp_le_i32_e64 s[20:21], v14, v0
	v_cndmask_b32_e32 v148, 0, v148, vcc
	v_cmp_le_i32_e32 vcc, v15, v0
	v_cndmask_b32_e64 v149, 0, v149, s[0:1]
	v_cndmask_b32_e64 v150, 0, v150, s[20:21]
	s_nop 0
	v_cndmask_b32_e32 v151, 0, v151, vcc
	v_sub_f32_e32 v152, v144, v137
	v_sub_f32_e32 v153, v145, v137
	v_sub_f32_e32 v154, v146, v137
	v_sub_f32_e32 v155, v147, v137
	v_mul_f32_e32 v152, s34, v152
	v_mul_f32_e32 v153, s34, v153
	v_mul_f32_e32 v154, s34, v154
	v_mul_f32_e32 v155, s34, v155
	v_exp_f32_e32 v152, v152
	v_exp_f32_e32 v153, v153
	v_exp_f32_e32 v154, v154
	v_exp_f32_e32 v155, v155
	s_waitcnt lgkmcnt(0)
	v_mfma_f32_16x16x32_bf16 v[128:131], v[40:43], v[88:91], 0
	v_mfma_f32_16x16x32_bf16 v[128:131], v[44:47], v[92:95], v[128:131]
	v_mfma_f32_16x16x32_bf16 v[128:131], v[48:51], v[96:99], v[128:131]
	v_mfma_f32_16x16x32_bf16 v[128:131], v[52:55], v[100:103], v[128:131]
	v_mul_f32_e32 v152, v124, v152
	v_mul_f32_e32 v153, v125, v153
	v_mul_f32_e32 v154, v126, v154
	v_mul_f32_e32 v155, v127, v155
	v_sub_f32_e32 v156, v144, v138
	v_sub_f32_e32 v157, v145, v138
	v_sub_f32_e32 v158, v146, v138
	v_sub_f32_e32 v159, v147, v138
	v_mul_f32_e32 v156, s34, v156
	v_mul_f32_e32 v157, s34, v157
	v_mul_f32_e32 v158, s34, v158
	v_mul_f32_e32 v159, s34, v159
	v_exp_f32_e32 v156, v156
	v_exp_f32_e32 v157, v157
	v_exp_f32_e32 v158, v158
	v_exp_f32_e32 v159, v159
	v_mul_f32_e32 v156, v128, v156
	v_mul_f32_e32 v157, v129, v157
	v_mul_f32_e32 v158, v130, v158
	v_mul_f32_e32 v159, v131, v159
	v_cvt_pk_bf16_f32 v164, v148, v149
	v_cvt_pk_bf16_f32 v165, v150, v151
	v_cvt_pk_bf16_f32 v166, v152, v153
	v_cvt_pk_bf16_f32 v167, v154, v155
	v_cvt_pk_bf16_f32 v168, v156, v157
	v_cvt_pk_bf16_f32 v169, v158, v159
	v_add_u32_e32 v17, 0x1000, v7
	global_store_dwordx2 v7, v[164:165], s[2:3]
	global_store_dwordx2 v7, v[166:167], s[2:3] offset:256
	global_store_dwordx2 v17, v[168:169], s[2:3]
	s_branch .Lgc_join
.Lgc_w5:
	s_mov_b32 s34, 0xbfb8aa3b
	v_add_u32_e32 v3, 0x0, v4
	v_add_u32_e32 v2, 0x8800, v4
	v_lshlrev_b32_e32 v5, 4, v1
	v_add_u32_e32 v5, 0x1c400, v5
	ds_read_b128 v[40:43], v3
	ds_read_b128 v[44:47], v3 offset:64
	ds_read_b128 v[48:51], v3 offset:128
	ds_read_b128 v[52:55], v3 offset:192
	ds_read_b128 v[104:107], v2 offset:13056
	ds_read_b128 v[108:111], v2 offset:13120
	ds_read_b128 v[112:115], v2 offset:13184
	ds_read_b128 v[116:119], v2 offset:13248
	ds_read_b128 v[144:147], v5
	ds_read_b32 v139, v6 offset:192
	s_waitcnt lgkmcnt(0)
	v_mfma_f32_16x16x32_bf16 v[132:135], v[40:43], v[104:107], 0
	v_mfma_f32_16x16x32_bf16 v[132:135], v[44:47], v[108:111], v[132:135]
	v_mfma_f32_16x16x32_bf16 v[132:135], v[48:51], v[112:115], v[132:135]
	v_mfma_f32_16x16x32_bf16 v[132:135], v[52:55], v[116:119], v[132:135]
	v_sub_f32_e32 v160, v144, v139
	v_sub_f32_e32 v161, v145, v139
	v_sub_f32_e32 v162, v146, v139
	v_sub_f32_e32 v163, v147, v139
	v_mul_f32_e32 v160, s34, v160
	v_mul_f32_e32 v161, s34, v161
	v_mul_f32_e32 v162, s34, v162
	v_mul_f32_e32 v163, s34, v163
	v_exp_f32_e32 v160, v160
	v_exp_f32_e32 v161, v161
	v_exp_f32_e32 v162, v162
	v_exp_f32_e32 v163, v163
	v_mul_f32_e32 v160, v132, v160
	v_mul_f32_e32 v161, v133, v161
	v_mul_f32_e32 v162, v134, v162
	v_mul_f32_e32 v163, v135, v163
	v_cvt_pk_bf16_f32 v170, v160, v161
	v_cvt_pk_bf16_f32 v171, v162, v163
	v_add_u32_e32 v17, 0x1000, v7
	global_store_dwordx2 v17, v[170:171], s[2:3] offset:256
	s_mov_b32 s34, 0xbfb8aa3b
	v_add_u32_e32 v3, 0x1100, v4
	v_add_u32_e32 v2, 0x8800, v4
	v_lshlrev_b32_e32 v5, 4, v1
	v_add_u32_e32 v5, 0x1c440, v5
	ds_read_b128 v[40:43], v3
	ds_read_b128 v[44:47], v3 offset:64
	ds_read_b128 v[48:51], v3 offset:128
	ds_read_b128 v[52:55], v3 offset:192
	ds_read_b128 v[72:75], v2 offset:4352
	ds_read_b128 v[76:79], v2 offset:4416
	ds_read_b128 v[80:83], v2 offset:4480
	ds_read_b128 v[84:87], v2 offset:4544
	ds_read_b128 v[144:147], v5
	ds_read_b32 v137, v6 offset:64
	ds_read_b32 v138, v6 offset:128
	ds_read_b128 v[88:91], v2 offset:8704
	ds_read_b128 v[92:95], v2 offset:8768
	ds_read_b128 v[96:99], v2 offset:8832
	ds_read_b128 v[100:103], v2 offset:8896
	v_add_u32_e32 v9, 16, v0
	v_lshl_add_u32 v12, v1, 2, 16
	v_add_u32_e32 v13, 1, v12
	v_add_u32_e32 v14, 2, v12
	v_add_u32_e32 v15, 3, v12
	s_waitcnt lgkmcnt(5)
	v_mfma_f32_16x16x32_bf16 v[124:127], v[40:43], v[72:75], 0
	v_mfma_f32_16x16x32_bf16 v[124:127], v[44:47], v[76:79], v[124:127]
	v_mfma_f32_16x16x32_bf16 v[124:127], v[48:51], v[80:83], v[124:127]
	v_mfma_f32_16x16x32_bf16 v[124:127], v[52:55], v[84:87], v[124:127]
	v_sub_f32_e32 v152, v144, v137
	v_sub_f32_e32 v153, v145, v137
	v_sub_f32_e32 v154, v146, v137
	v_sub_f32_e32 v155, v147, v137
	v_mul_f32_e32 v152, s34, v152
	v_mul_f32_e32 v153, s34, v153
	v_mul_f32_e32 v154, s34, v154
	v_mul_f32_e32 v155, s34, v155
	v_exp_f32_e32 v152, v152
	v_exp_f32_e32 v153, v153
	v_exp_f32_e32 v154, v154
	v_exp_f32_e32 v155, v155
	s_waitcnt lgkmcnt(0)
	v_mfma_f32_16x16x32_bf16 v[128:131], v[40:43], v[88:91], 0
	v_mfma_f32_16x16x32_bf16 v[128:131], v[44:47], v[92:95], v[128:131]
	v_mfma_f32_16x16x32_bf16 v[128:131], v[48:51], v[96:99], v[128:131]
	v_mfma_f32_16x16x32_bf16 v[128:131], v[52:55], v[100:103], v[128:131]
	v_mul_f32_e32 v152, v124, v152
	v_mul_f32_e32 v153, v125, v153
	v_mul_f32_e32 v154, v126, v154
	v_mul_f32_e32 v155, v127, v155
	v_cmp_le_i32_e32 vcc, v12, v9
	v_cmp_le_i32_e64 s[0:1], v13, v9
	v_cmp_le_i32_e64 s[20:21], v14, v9
	v_cndmask_b32_e32 v152, 0, v152, vcc
	v_cmp_le_i32_e32 vcc, v15, v9
	v_cndmask_b32_e64 v153, 0, v153, s[0:1]
	v_cndmask_b32_e64 v154, 0, v154, s[20:21]
	s_nop 0
	v_cndmask_b32_e32 v155, 0, v155, vcc
	v_sub_f32_e32 v156, v144, v138
	v_sub_f32_e32 v157, v145, v138
	v_sub_f32_e32 v158, v146, v138
	v_sub_f32_e32 v159, v147, v138
	v_mul_f32_e32 v156, s34, v156
	v_mul_f32_e32 v157, s34, v157
	v_mul_f32_e32 v158, s34, v158
	v_mul_f32_e32 v159, s34, v159
	v_exp_f32_e32 v156, v156
	v_exp_f32_e32 v157, v157
	v_exp_f32_e32 v158, v158
	v_exp_f32_e32 v159, v159
	v_mul_f32_e32 v156, v128, v156
	v_mul_f32_e32 v157, v129, v157
	v_mul_f32_e32 v158, v130, v158
	v_mul_f32_e32 v159, v131, v159
	v_cvt_pk_bf16_f32 v166, v152, v153
	v_cvt_pk_bf16_f32 v167, v154, v155
	v_cvt_pk_bf16_f32 v168, v156, v157
	v_cvt_pk_bf16_f32 v169, v158, v159
	v_add_u32_e32 v16, 0x400, v7
	v_add_u32_e32 v17, 0x1000, v16
	global_store_dwordx2 v16, v[166:167], s[2:3] offset:256
	global_store_dwordx2 v17, v[168:169], s[2:3]
	s_branch .Lgc_join
.Lgc_w6:
	s_mov_b32 s34, 0xbfb8aa3b
	v_add_u32_e32 v3, 0x1100, v4
	v_add_u32_e32 v2, 0x8800, v4
	v_lshlrev_b32_e32 v5, 4, v1
	v_add_u32_e32 v5, 0x1c440, v5
	ds_read_b128 v[40:43], v3
	ds_read_b128 v[44:47], v3 offset:64
	ds_read_b128 v[48:51], v3 offset:128
	ds_read_b128 v[52:55], v3 offset:192
	ds_read_b128 v[104:107], v2 offset:13056
	ds_read_b128 v[108:111], v2 offset:13120
	ds_read_b128 v[112:115], v2 offset:13184
	ds_read_b128 v[116:119], v2 offset:13248
	ds_read_b128 v[144:147], v5
	ds_read_b32 v139, v6 offset:192
	s_waitcnt lgkmcnt(0)
	v_mfma_f32_16x16x32_bf16 v[132:135], v[40:43], v[104:107], 0
	v_mfma_f32_16x16x32_bf16 v[132:135], v[44:47], v[108:111], v[132:135]
	v_mfma_f32_16x16x32_bf16 v[132:135], v[48:51], v[112:115], v[132:135]
	v_mfma_f32_16x16x32_bf16 v[132:135], v[52:55], v[116:119], v[132:135]
	v_sub_f32_e32 v160, v144, v139
	v_sub_f32_e32 v161, v145, v139
	v_sub_f32_e32 v162, v146, v139
	v_sub_f32_e32 v163, v147, v139
	v_mul_f32_e32 v160, s34, v160
	v_mul_f32_e32 v161, s34, v161
	v_mul_f32_e32 v162, s34, v162
	v_mul_f32_e32 v163, s34, v163
	v_exp_f32_e32 v160, v160
	v_exp_f32_e32 v161, v161
	v_exp_f32_e32 v162, v162
	v_exp_f32_e32 v163, v163
	v_mul_f32_e32 v160, v132, v160
	v_mul_f32_e32 v161, v133, v161
	v_mul_f32_e32 v162, v134, v162
	v_mul_f32_e32 v163, v135, v163
	v_cvt_pk_bf16_f32 v170, v160, v161
	v_cvt_pk_bf16_f32 v171, v162, v163
	v_add_u32_e32 v16, 0x400, v7
	v_add_u32_e32 v17, 0x1000, v16
	global_store_dwordx2 v17, v[170:171], s[2:3] offset:256
	s_mov_b32 s34, 0xbfb8aa3b
	v_add_u32_e32 v3, 0x2200, v4
	v_add_u32_e32 v2, 0x8800, v4
	v_lshlrev_b32_e32 v5, 4, v1
	v_add_u32_e32 v5, 0x1c480, v5
	ds_read_b128 v[40:43], v3
	ds_read_b128 v[44:47], v3 offset:64
	ds_read_b128 v[48:51], v3 offset:128
	ds_read_b128 v[52:55], v3 offset:192
	ds_read_b128 v[88:91], v2 offset:8704
	ds_read_b128 v[92:95], v2 offset:8768
	ds_read_b128 v[96:99], v2 offset:8832
	ds_read_b128 v[100:103], v2 offset:8896
	ds_read_b128 v[144:147], v5
	ds_read_b32 v138, v6 offset:128
	ds_read_b32 v139, v6 offset:192
	ds_read_b128 v[104:107], v2 offset:13056
	ds_read_b128 v[108:111], v2 offset:13120
	ds_read_b128 v[112:115], v2 offset:13184
	ds_read_b128 v[116:119], v2 offset:13248
	v_add_u32_e32 v10, 32, v0
	v_lshl_add_u32 v12, v1, 2, 32
	v_add_u32_e32 v13, 1, v12
	v_add_u32_e32 v14, 2, v12
	v_add_u32_e32 v15, 3, v12
	s_waitcnt lgkmcnt(5)
	v_mfma_f32_16x16x32_bf16 v[128:131], v[40:43], v[88:91], 0
	v_mfma_f32_16x16x32_bf16 v[128:131], v[44:47], v[92:95], v[128:131]
	v_mfma_f32_16x16x32_bf16 v[128:131], v[48:51], v[96:99], v[128:131]
	v_mfma_f32_16x16x32_bf16 v[128:131], v[52:55], v[100:103], v[128:131]
	v_sub_f32_e32 v156, v144, v138
	v_sub_f32_e32 v157, v145, v138
	v_sub_f32_e32 v158, v146, v138
	v_sub_f32_e32 v159, v147, v138
	v_mul_f32_e32 v156, s34, v156
	v_mul_f32_e32 v157, s34, v157
	v_mul_f32_e32 v158, s34, v158
	v_mul_f32_e32 v159, s34, v159
	v_exp_f32_e32 v156, v156
	v_exp_f32_e32 v157, v157
	v_exp_f32_e32 v158, v158
	v_exp_f32_e32 v159, v159
	s_waitcnt lgkmcnt(0)
	v_mfma_f32_16x16x32_bf16 v[132:135], v[40:43], v[104:107], 0
	v_mfma_f32_16x16x32_bf16 v[132:135], v[44:47], v[108:111], v[132:135]
	v_mfma_f32_16x16x32_bf16 v[132:135], v[48:51], v[112:115], v[132:135]
	v_mfma_f32_16x16x32_bf16 v[132:135], v[52:55], v[116:119], v[132:135]
	v_mul_f32_e32 v156, v128, v156
	v_mul_f32_e32 v157, v129, v157
	v_mul_f32_e32 v158, v130, v158
	v_mul_f32_e32 v159, v131, v159
	v_cmp_le_i32_e32 vcc, v12, v10
	v_cmp_le_i32_e64 s[0:1], v13, v10
	v_cmp_le_i32_e64 s[20:21], v14, v10
	v_cndmask_b32_e32 v156, 0, v156, vcc
	v_cmp_le_i32_e32 vcc, v15, v10
	v_cndmask_b32_e64 v157, 0, v157, s[0:1]
	v_cndmask_b32_e64 v158, 0, v158, s[20:21]
	s_nop 0
	v_cndmask_b32_e32 v159, 0, v159, vcc
	v_sub_f32_e32 v160, v144, v139
	v_sub_f32_e32 v161, v145, v139
	v_sub_f32_e32 v162, v146, v139
	v_sub_f32_e32 v163, v147, v139
	v_mul_f32_e32 v160, s34, v160
	v_mul_f32_e32 v161, s34, v161
	v_mul_f32_e32 v162, s34, v162
	v_mul_f32_e32 v163, s34, v163
	v_exp_f32_e32 v160, v160
	v_exp_f32_e32 v161, v161
	v_exp_f32_e32 v162, v162
	v_exp_f32_e32 v163, v163
	v_mul_f32_e32 v160, v132, v160
	v_mul_f32_e32 v161, v133, v161
	v_mul_f32_e32 v162, v134, v162
	v_mul_f32_e32 v163, v135, v163
	v_cvt_pk_bf16_f32 v168, v156, v157
	v_cvt_pk_bf16_f32 v169, v158, v159
	v_cvt_pk_bf16_f32 v170, v160, v161
	v_cvt_pk_bf16_f32 v171, v162, v163
	v_add_u32_e32 v16, 0x800, v7
	v_add_u32_e32 v17, 0x1000, v16
	global_store_dwordx2 v17, v[168:169], s[2:3]
	global_store_dwordx2 v17, v[170:171], s[2:3] offset:256
	s_branch .Lgc_join
.Lgc_w7:
	s_mov_b32 s34, 0x3fb8aa3b
	v_add_u32_e32 v3, 0x6600, v4
	v_lshlrev_b32_e32 v5, 4, v1
	v_add_u32_e32 v5, 0x1c480, v5
	ds_read_b128 v[40:43], v3
	ds_read_b128 v[44:47], v3 offset:64
	ds_read_b128 v[48:51], v3 offset:128
	ds_read_b128 v[52:55], v3 offset:192
	ds_read_b128 v[88:91], v4 offset:8704
	ds_read_b128 v[92:95], v4 offset:8768
	ds_read_b128 v[96:99], v4 offset:8832
	ds_read_b128 v[100:103], v4 offset:8896
	ds_read_b128 v[144:147], v5
	ds_read_b32 v138, v6 offset:128
	v_add_u32_e32 v10, 32, v0
	v_lshl_add_u32 v12, v1, 2, 32
	v_add_u32_e32 v13, 1, v12
	v_add_u32_e32 v14, 2, v12
	v_add_u32_e32 v15, 3, v12
	s_waitcnt lgkmcnt(0)
	v_mfma_f32_16x16x32_bf16 v[128:131], v[40:43], v[88:91], 0
	v_mfma_f32_16x16x32_bf16 v[128:131], v[44:47], v[92:95], v[128:131]
	v_mfma_f32_16x16x32_bf16 v[128:131], v[48:51], v[96:99], v[128:131]
	v_mfma_f32_16x16x32_bf16 v[128:131], v[52:55], v[100:103], v[128:131]
	v_sub_f32_e32 v156, v144, v138
	v_sub_f32_e32 v157, v145, v138
	v_sub_f32_e32 v158, v146, v138
	v_sub_f32_e32 v159, v147, v138
	v_mul_f32_e32 v156, s34, v156
	v_mul_f32_e32 v157, s34, v157
	v_mul_f32_e32 v158, s34, v158
	v_mul_f32_e32 v159, s34, v159
	v_exp_f32_e32 v156, v156
	v_exp_f32_e32 v157, v157
	v_exp_f32_e32 v158, v158
	v_exp_f32_e32 v159, v159
	v_mul_f32_e32 v156, v128, v156
	v_mul_f32_e32 v157, v129, v157
	v_mul_f32_e32 v158, v130, v158
	v_mul_f32_e32 v159, v131, v159
	v_cmp_lt_i32_e32 vcc, v10, v12
	v_cmp_lt_i32_e64 s[0:1], v10, v13
	v_cmp_lt_i32_e64 s[20:21], v10, v14
	v_cndmask_b32_e32 v156, 0, v156, vcc
	v_cmp_lt_i32_e32 vcc, v10, v15
	v_cndmask_b32_e64 v157, 0, v157, s[0:1]
	v_cndmask_b32_e64 v158, 0, v158, s[20:21]
	s_nop 0
	v_cndmask_b32_e32 v159, 0, v159, vcc
	v_add_u32_e32 v16, 0x15c80, v4
	ds_write_b128 v16, v[156:159] offset:8704
	s_mov_b32 s34, 0x3fb8aa3b
	v_add_u32_e32 v3, 0x7700, v4
	v_lshlrev_b32_e32 v5, 4, v1
	v_add_u32_e32 v5, 0x1c4c0, v5
	ds_read_b128 v[40:43], v3
	ds_read_b128 v[44:47], v3 offset:64
	ds_read_b128 v[48:51], v3 offset:128
	ds_read_b128 v[52:55], v3 offset:192
	ds_read_b128 v[104:107], v4 offset:13056
	ds_read_b128 v[108:111], v4 offset:13120
	ds_read_b128 v[112:115], v4 offset:13184
	ds_read_b128 v[116:119], v4 offset:13248
	ds_read_b128 v[144:147], v5
	ds_read_b32 v139, v6 offset:192
	v_add_u32_e32 v11, 48, v0
	v_lshl_add_u32 v12, v1, 2, 48
	v_add_u32_e32 v13, 1, v12
	v_add_u32_e32 v14, 2, v12
	v_add_u32_e32 v15, 3, v12
	s_waitcnt lgkmcnt(0)
	v_mfma_f32_16x16x32_bf16 v[132:135], v[40:43], v[104:107], 0
	v_mfma_f32_16x16x32_bf16 v[132:135], v[44:47], v[108:111], v[132:135]
	v_mfma_f32_16x16x32_bf16 v[132:135], v[48:51], v[112:115], v[132:135]
	v_mfma_f32_16x16x32_bf16 v[132:135], v[52:55], v[116:119], v[132:135]
	v_sub_f32_e32 v160, v144, v139
	v_sub_f32_e32 v161, v145, v139
	v_sub_f32_e32 v162, v146, v139
	v_sub_f32_e32 v163, v147, v139
	v_mul_f32_e32 v160, s34, v160
	v_mul_f32_e32 v161, s34, v161
	v_mul_f32_e32 v162, s34, v162
	v_mul_f32_e32 v163, s34, v163
	v_exp_f32_e32 v160, v160
	v_exp_f32_e32 v161, v161
	v_exp_f32_e32 v162, v162
	v_exp_f32_e32 v163, v163
	v_mul_f32_e32 v160, v132, v160
	v_mul_f32_e32 v161, v133, v161
	v_mul_f32_e32 v162, v134, v162
	v_mul_f32_e32 v163, v135, v163
	v_cmp_lt_i32_e32 vcc, v11, v12
	v_cmp_lt_i32_e64 s[0:1], v11, v13
	v_cmp_lt_i32_e64 s[20:21], v11, v14
	v_cndmask_b32_e32 v160, 0, v160, vcc
	v_cmp_lt_i32_e32 vcc, v11, v15
	v_cndmask_b32_e64 v161, 0, v161, s[0:1]
	v_cndmask_b32_e64 v162, 0, v162, s[20:21]
	s_nop 0
	v_cndmask_b32_e32 v163, 0, v163, vcc
	v_add_u32_e32 v16, 0x15cc0, v4
	ds_write_b128 v16, v[160:163] offset:13056
	v_mov_b32_e32 v164, 0
	v_mov_b32_e32 v165, 0
	v_add_u32_e32 v16, 0x400, v7
	global_store_dwordx2 v16, v[164:165], s[2:3]
	v_add_u32_e32 v16, 0x800, v7
	global_store_dwordx2 v16, v[164:165], s[2:3]
	global_store_dwordx2 v16, v[164:165], s[2:3] offset:256
	v_add_u32_e32 v16, 0xc00, v7
	v_add_u32_e32 v17, 0x1000, v16
	global_store_dwordx2 v16, v[164:165], s[2:3]
	global_store_dwordx2 v16, v[164:165], s[2:3] offset:256
	global_store_dwordx2 v17, v[164:165], s[2:3]
	s_branch .Lgc_join
